# LDS/global latency overlap: dilated attention K-fragment reads of tiles 1-4 pipelined, output-row LDS reads issued together, loop-top vmcnt relaxed to 4; pool weight-tile loads issued with the row loa
# speedup vs baseline: 1.0085x; 1.0049x over previous
.LBB0_540:
	v_ashrrev_i32_e32 v0, 2, v194
	v_bfe_u32 v210, v192, 3, 5
	s_waitcnt vmcnt(0)
	v_lshrrev_b32_e32 v2, 4, v192
	v_lshlrev_b32_e32 v3, 2, v192
	v_lshlrev_b32_e32 v4, 1, v194
	v_and_b32_e32 v5, 7, v194
	v_readlane_b32 s4, v253, 23
	s_cmpk_gt_i32 s72, 0x5ff
	v_add_u32_e32 v173, 0x800, v192
	v_ashrrev_i32_e32 v211, 8, v192
	v_lshrrev_b32_e32 v193, 2, v194
	v_and_b32_e32 v162, -8, v0
	v_lshl_add_u32 v207, v210, 7, 0
	v_xor_b32_e32 v209, v2, v194
	v_and_b32_e32 v208, 64, v3
	v_and_b32_e32 v195, 32, v4
	v_lshl_add_u32 v206, v5, 4, s4
	v_lshlrev_b32_e32 v172, 3, v5
	s_cbranch_scc1 .LBB0_559
	s_waitcnt lgkmcnt(0)
	s_add_u32 s5, s52, 0x4b000000
	s_addc_u32 s14, s53, 0
	s_add_u32 s15, s52, 0x20000000
	s_addc_u32 s16, s53, 0
	s_add_u32 s17, s52, 0x1800000
	s_addc_u32 s30, s53, 0
	s_ashr_i32 s4, s72, 5
	s_mul_hi_i32 s6, s4, 0x55555556
	s_lshr_b32 s26, s6, 31
	s_add_i32 s40, s6, s26
	s_mul_i32 s6, s40, 3
	s_sub_i32 s38, s4, s6
	s_ashr_i32 s39, s38, 31
	s_lshl_b64 s[26:27], s[38:39], 19
	s_add_u32 s4, s17, s26
	s_addc_u32 s6, s30, s27
	s_ashr_i32 s36, s40, 3
	s_ashr_i32 s37, s36, 31
	s_lshl_b64 s[26:27], s[36:37], 18
	s_add_u32 s4, s4, s26
	s_addc_u32 s6, s6, s27
	s_and_b32 s31, s40, 7
	s_lshl_b32 s26, s31, 2
	s_add_u32 s26, s4, s26
	s_addc_u32 s27, s6, 0
	s_lshl_b64 s[42:43], s[38:39], 24
	s_add_u32 s4, s15, s42
	s_addc_u32 s6, s16, s43
	s_lshl_b64 s[36:37], s[36:37], 23
	s_add_u32 s4, s4, s36
	s_addc_u32 s6, s6, s37
	s_lshl_b32 s31, s31, 7
	s_add_u32 s36, s4, s31
	s_addc_u32 s37, s6, 0
	s_ashr_i32 s41, s40, 31
	s_lshl_b64 s[42:43], s[40:41], 20
	s_add_u32 s42, s5, s42
	s_addc_u32 s43, s14, s43
	s_cmp_eq_u32 s38, 1
	s_cselect_b32 s4, 4, 16
	s_cselect_b32 s6, 2, 4
	s_cmp_eq_u32 s38, 0
	s_cselect_b32 s6, 0, s6
	s_cselect_b32 s31, 1, s4
	s_lshr_b32 s4, 32, s6
	s_add_i32 s4, s4, -1
	s_and_b32 s38, s72, 31
	s_and_b32 s4, s4, s38
	s_lshl_b32 s39, s4, 8
	s_sub_i32 s41, 5, s6
	s_lshl_b32 s39, s39, s6
	s_lshr_b32 s44, s38, s41
	s_add_i32 s38, s40, 32
	s_waitcnt vmcnt(14)
	v_and_b32_e32 v8, 31, v194
	v_readlane_b32 s45, v253, 20
	s_or_b32 s75, s39, s44
	s_ashr_i32 s39, s38, 31
	v_or_b32_e32 v147, s45, v8
	s_lshl_b64 s[38:39], s[38:39], 20
	v_lshlrev_b32_e32 v0, s6, v147
	s_add_u32 s38, s5, s38
	v_add_u32_e32 v2, s75, v0
	s_addc_u32 s39, s14, s39
	v_add_u32_e32 v0, 0xa00, v192
	s_lshl_b32 s4, s4, 3
	v_ashrrev_i32_e32 v3, 31, v2
	v_ashrrev_i32_e32 v212, 8, v0
	s_add_i32 s4, s4, -2
	v_lshlrev_b64 v[2:3], 7, v[2:3]
	v_add_u32_e32 v0, s4, v212
	s_lshr_b32 s94, 0x100, s6
	v_lshl_add_u64 v[2:3], s[42:43], 0, v[2:3]
	v_max_i32_e32 v0, 0, v0
	s_add_i32 s42, s94, -1
	v_min_u32_e32 v0, s42, v0
	v_lshl_or_b32 v0, v0, 5, v210
	v_lshlrev_b32_e32 v0, s6, v0
	v_ashrrev_i32_e32 v163, 31, v162
	v_add_u32_e32 v0, s44, v0
	v_ashrrev_i32_e32 v213, 8, v173
	v_lshl_add_u64 v[2:3], v[162:163], 1, v[2:3]
	v_lshlrev_b64 v[4:5], 7, v[0:1]
	s_add_i32 s40, s40, 16
	v_add_u32_e32 v0, s4, v213
	global_load_dwordx4 v[130:133], v[2:3], off offset:96
	global_load_dwordx4 v[134:137], v[2:3], off offset:64
	global_load_dwordx4 v[138:141], v[2:3], off offset:32
	global_load_dwordx4 v[142:145], v[2:3], off
	v_lshlrev_b32_e32 v3, 3, v194
	s_ashr_i32 s41, s40, 31
	v_max_i32_e32 v0, 0, v0
	v_and_b32_e32 v2, 56, v3
	s_lshl_b64 s[40:41], s[40:41], 20
	v_min_u32_e32 v0, s42, v0
	v_lshlrev_b32_e32 v9, 1, v2
	s_add_u32 s40, s5, s40
	v_lshl_or_b32 v0, v0, 5, v210
	v_or_b32_e32 v4, v4, v9
	s_addc_u32 s41, s14, s41
	v_lshlrev_b32_e32 v0, s6, v0
	v_lshl_add_u64 v[6:7], s[38:39], 0, v[4:5]
	v_lshl_add_u64 v[4:5], s[40:41], 0, v[4:5]
	v_add_u32_e32 v0, s44, v0
	global_load_dwordx4 v[66:69], v[6:7], off
	global_load_dwordx4 v[70:73], v[4:5], off
	v_lshlrev_b64 v[4:5], 7, v[0:1]
	v_add_u32_e32 v0, 0x600, v192
	v_ashrrev_i32_e32 v214, 8, v0
	v_add_u32_e32 v0, s4, v214
	v_max_i32_e32 v0, 0, v0
	v_min_u32_e32 v0, s42, v0
	v_lshl_or_b32 v0, v0, 5, v210
	v_or_b32_e32 v4, v4, v9
	v_lshlrev_b32_e32 v0, s6, v0
	v_lshl_add_u64 v[6:7], s[38:39], 0, v[4:5]
	v_lshl_add_u64 v[4:5], s[40:41], 0, v[4:5]
	v_add_u32_e32 v0, s44, v0
	global_load_dwordx4 v[74:77], v[6:7], off
	global_load_dwordx4 v[78:81], v[4:5], off
	v_lshlrev_b64 v[4:5], 7, v[0:1]
	v_add_u32_e32 v0, 0x400, v192
	v_ashrrev_i32_e32 v215, 8, v0
	v_add_u32_e32 v0, s4, v215
	v_max_i32_e32 v0, 0, v0
	v_min_u32_e32 v0, s42, v0
	v_lshl_or_b32 v0, v0, 5, v210
	v_or_b32_e32 v4, v4, v9
	v_lshlrev_b32_e32 v0, s6, v0
	v_lshl_add_u64 v[6:7], s[38:39], 0, v[4:5]
	v_lshl_add_u64 v[4:5], s[40:41], 0, v[4:5]
	v_add_u32_e32 v0, s44, v0
	global_load_dwordx4 v[82:85], v[6:7], off
	global_load_dwordx4 v[86:89], v[4:5], off
	v_lshlrev_b64 v[4:5], 7, v[0:1]
	v_add_u32_e32 v0, 0x200, v192
	v_ashrrev_i32_e32 v216, 8, v0
	v_add_u32_e32 v0, s4, v216
	v_max_i32_e32 v0, 0, v0
	v_min_u32_e32 v0, s42, v0
	v_lshl_or_b32 v0, v0, 5, v210
	v_or_b32_e32 v4, v4, v9
	v_lshlrev_b32_e32 v0, s6, v0
	v_lshl_add_u64 v[6:7], s[38:39], 0, v[4:5]
	v_lshl_add_u64 v[4:5], s[40:41], 0, v[4:5]
	v_add_u32_e32 v0, s44, v0
	global_load_dwordx4 v[90:93], v[6:7], off
	global_load_dwordx4 v[94:97], v[4:5], off
	v_lshlrev_b64 v[4:5], 7, v[0:1]
	v_add_u32_e32 v0, s4, v211
	v_max_i32_e32 v0, 0, v0
	v_min_u32_e32 v0, s42, v0
	v_lshl_or_b32 v0, v0, 5, v210
	v_or_b32_e32 v4, v4, v9
	v_lshlrev_b32_e32 v0, s6, v0
	v_lshl_add_u64 v[6:7], s[38:39], 0, v[4:5]
	v_lshl_add_u64 v[4:5], s[40:41], 0, v[4:5]
	v_add_u32_e32 v0, s44, v0
	global_load_dwordx4 v[98:101], v[6:7], off
	global_load_dwordx4 v[106:109], v[4:5], off
	v_lshlrev_b64 v[4:5], 7, v[0:1]
	v_or_b32_e32 v4, v4, v9
	v_lshl_add_u64 v[6:7], s[38:39], 0, v[4:5]
	v_lshl_add_u64 v[4:5], s[40:41], 0, v[4:5]
	global_load_dwordx4 v[102:105], v[6:7], off
	global_load_dwordx4 v[110:113], v[4:5], off
	v_ashrrev_i32_e32 v9, 5, v194
	s_waitcnt vmcnt(29)
	v_lshlrev_b32_e32 v13, 2, v9
	s_waitcnt vmcnt(28)
	v_and_or_b32 v14, v193, 3, v13
	v_lshlrev_b32_e32 v0, 4, v192
	v_lshlrev_b32_e32 v4, 4, v209
	v_lshrrev_b32_e32 v10, 1, v194
	v_lshlrev_b32_e32 v11, 7, v8
	v_readlane_b32 s6, v253, 22
	v_lshlrev_b32_e32 v14, 7, v14
	v_and_b32_e32 v15, 24, v3
	v_readlane_b32 s38, v253, 21
	v_and_b32_e32 v3, 64, v3
	v_add_u32_e32 v17, 2, v9
	s_waitcnt vmcnt(27)
	v_add_u32_e32 v18, 4, v9
	v_add_u32_e32 v19, 6, v9
	v_ashrrev_i32_e32 v223, 3, v194
	v_writelane_b32 v255, s54, 9
	v_and_b32_e32 v4, 0x70, v4
	v_and_b32_e32 v5, 0x70, v0
	v_and_b32_e32 v218, 0xfffff000, v0
	v_or_b32_e32 v12, s6, v11
	v_add_u32_e32 v16, s38, v14
	v_or3_b32 v3, v195, v15, v3
	v_bitop3_b32 v15, v10, v9, 7 bitop3:0x6c
	v_bitop3_b32 v17, v17, v10, 7 bitop3:0x78
	v_bitop3_b32 v18, v18, v10, 7 bitop3:0x78
	v_bitop3_b32 v10, v19, v10, 7 bitop3:0x78
	v_sub_u32_e32 v219, v8, v13
	v_add_u32_e32 v8, s6, v14
	v_readlane_b32 s6, v253, 23
	v_lshlrev_b32_e32 v233, 7, v223
	v_writelane_b32 v255, s82, 10
	v_add_u32_e32 v4, v207, v4
	v_xad_u32 v217, v208, v5, v207
	v_add_u32_e32 v0, 0x4000, v218
	v_add_u32_e32 v5, 0x6000, v218
	v_add_u32_e32 v6, 0x8000, v218
	v_add_u32_e32 v7, 0xa000, v218
	v_lshl_add_u32 v15, v15, 4, v12
	v_lshl_add_u32 v17, v17, 4, v12
	v_lshl_add_u32 v18, v18, 4, v12
	v_lshl_add_u32 v10, v10, 4, v12
	v_bitop3_b32 v12, v16, 64, v3 bitop3:0x36
	v_add3_u32 v220, v8, v3, 0
	v_add_u32_e32 v3, s6, v11
	v_lshlrev_b32_e32 v8, 3, v9
	v_add_u32_e32 v9, 0x400, v233
	v_add_u32_e32 v11, 0x800, v233
	v_add_u32_e32 v13, 0xc00, v233
	s_waitcnt vmcnt(12)
	v_mov_b64_e32 v[114:115], v[142:143]
	v_mov_b64_e32 v[118:119], v[138:139]
	v_mov_b64_e32 v[122:123], v[134:135]
	v_mov_b64_e32 v[126:127], v[130:131]
	v_writelane_b32 v255, s83, 11
	v_add_u32_e32 v221, 0xd000, v220
	v_cmp_gt_u32_e64 s[38:39], 32, v194
	v_add_u32_e32 v222, s45, v194
	v_add_u32_e32 v234, v4, v218
	v_add_u32_e32 v235, v217, v0
	v_add_u32_e32 v236, v217, v5
	v_add_u32_e32 v237, v217, v6
	v_add_u32_e32 v238, v217, v7
	v_lshlrev_b32_e32 v239, 1, v2
	v_add_u32_e32 v240, v3, v8
	v_lshlrev_b32_e32 v0, 1, v172
	v_add_u32_e32 v241, v206, v9
	v_add_u32_e32 v242, v206, v11
	v_add_u32_e32 v243, v206, v13
	v_add_u32_e32 v244, 0, v15
	v_add_u32_e32 v245, 0, v17
	v_add_u32_e32 v246, 0, v18
	v_add_u32_e32 v247, 0, v10
	v_add_u32_e32 v248, 0, v12
	s_mov_b32 s84, s72
	v_mov_b64_e32 v[116:117], v[144:145]
	v_mov_b64_e32 v[120:121], v[140:141]
	v_mov_b64_e32 v[124:125], v[136:137]
	v_mov_b64_e32 v[128:129], v[132:133]
	s_mov_b64 s[82:83], s[26:27]
	s_mov_b64 s[92:93], s[36:37]
	s_mov_b32 s85, s94
	s_mov_b32 s6, s4
	s_mov_b32 s73, s31
	s_mov_b32 s74, s75
	s_waitcnt vmcnt(0)
	s_branch .LBB0_543
.LBB0_542:
	s_or_b64 exec, exec, s[40:41]
	v_readlane_b32 s4, v253, 20
	s_mul_i32 s4, s31, s4
	s_waitcnt lgkmcnt(0)
	s_add_i32 s94, s4, s75
	v_add_u32_e32 v2, v206, v233
	ds_read_b128 v[2:5], v2
	ds_read_b128 v[10:13], v241
	ds_read_b128 v[14:17], v242
	ds_read_b128 v[18:21], v243
	s_lshl_b64 s[26:27], s[94:95], 10
	v_mul_lo_u32 v6, s31, v223
	s_add_u32 s26, s36, s26
	v_ashrrev_i32_e32 v7, 31, v6
	s_addc_u32 s27, s37, s27
	v_lshlrev_b64 v[8:9], 10, v[6:7]
	v_lshl_add_u64 v[8:9], s[26:27], 0, v[8:9]
	v_lshl_add_u64 v[8:9], v[8:9], 0, v[0:1]
	s_lshl_b32 s4, s31, 3
	s_waitcnt lgkmcnt(3)
	global_store_dwordx4 v[8:9], v[2:5], off
	v_add_u32_e32 v6, s4, v6
	v_ashrrev_i32_e32 v7, 31, v6
	v_lshlrev_b64 v[8:9], 10, v[6:7]
	v_lshl_add_u64 v[8:9], s[26:27], 0, v[8:9]
	v_lshl_add_u64 v[8:9], v[8:9], 0, v[0:1]
	s_waitcnt lgkmcnt(2)
	global_store_dwordx4 v[8:9], v[10:13], off
	v_add_u32_e32 v6, s4, v6
	v_ashrrev_i32_e32 v7, 31, v6
	v_lshlrev_b64 v[8:9], 10, v[6:7]
	v_lshl_add_u64 v[8:9], s[26:27], 0, v[8:9]
	v_lshl_add_u64 v[8:9], v[8:9], 0, v[0:1]
	s_waitcnt lgkmcnt(1)
	global_store_dwordx4 v[8:9], v[14:17], off
	v_add_u32_e32 v6, s4, v6
	v_ashrrev_i32_e32 v7, 31, v6
	v_lshlrev_b64 v[6:7], 10, v[6:7]
	v_lshl_add_u64 v[6:7], s[26:27], 0, v[6:7]
	s_waitcnt vmcnt(6)
	v_mov_b64_e32 v[144:145], v[116:117]
	s_waitcnt vmcnt(5)
	v_mov_b64_e32 v[140:141], v[120:121]
	s_waitcnt vmcnt(4)
	v_mov_b64_e32 v[136:137], v[124:125]
	s_waitcnt vmcnt(3)
	v_mov_b64_e32 v[132:133], v[128:129]
	v_lshl_add_u64 v[6:7], v[6:7], 0, v[0:1]
	s_and_b64 vcc, exec, s[78:79]
	v_mov_b64_e32 v[142:143], v[114:115]
	v_mov_b64_e32 v[138:139], v[118:119]
	v_mov_b64_e32 v[134:135], v[122:123]
	v_mov_b64_e32 v[130:131], v[126:127]
	s_mov_b64 s[26:27], s[82:83]
	s_mov_b64 s[36:37], s[92:93]
	s_mov_b32 s75, s74
	s_mov_b32 s31, s73
	s_mov_b32 s4, s6
	s_mov_b32 s94, s85
	s_waitcnt lgkmcnt(0)
	global_store_dwordx4 v[6:7], v[18:21], off
	s_cbranch_vccnz .LBB0_571
.LBB0_543:
	s_add_i32 s84, s84, s76
	s_cmpk_gt_i32 s84, 0x5ff
	s_cselect_b64 s[78:79], -1, 0
	v_add_u32_e32 v2, v217, v218
	s_and_b64 vcc, exec, s[78:79]
	s_barrier
	s_waitcnt vmcnt(4)
	ds_write_b128 v234, v[110:113]
	ds_write_b128 v2, v[102:105] offset:49152
	ds_write_b128 v234, v[106:109] offset:8192
	ds_write_b128 v2, v[98:101] offset:57344
	ds_write_b128 v234, v[94:97] offset:16384
	ds_write_b128 v235, v[90:93] offset:49152
	ds_write_b128 v234, v[86:89] offset:24576
	ds_write_b128 v236, v[82:85] offset:49152
	ds_write_b128 v234, v[78:81] offset:32768
	ds_write_b128 v237, v[74:77] offset:49152
	ds_write_b128 v234, v[70:73] offset:40960
	ds_write_b128 v238, v[66:69] offset:49152
	s_waitcnt lgkmcnt(0)
	s_barrier
	s_cbranch_vccnz .LBB0_545
	s_ashr_i32 s6, s84, 5
	s_mul_hi_i32 s40, s6, 0x55555556
	s_lshr_b32 s41, s40, 31
	s_add_i32 s48, s40, s41
	s_mul_i32 s40, s48, 3
	s_sub_i32 s40, s6, s40
	s_ashr_i32 s42, s48, 3
	s_and_b32 s50, s48, 7
	s_and_b32 s6, s84, 31
	s_cmp_eq_u32 s40, 1
	s_cselect_b32 s41, 4, 16
	s_cselect_b32 s43, 2, 4
	s_cmp_eq_u32 s40, 0
	s_cselect_b32 s43, 0, s43
	s_cselect_b32 s73, 1, s41
	s_lshr_b32 s41, 32, s43
	s_sub_i32 s44, 5, s43
	s_add_i32 s41, s41, -1
	s_lshr_b32 s51, s6, s44
	s_and_b32 s6, s41, s6
	s_ashr_i32 s49, s48, 31
	s_lshr_b32 s85, 0x100, s43
	s_lshl_b32 s41, s6, 3
	s_lshl_b64 s[44:45], s[48:49], 20
	s_add_u32 s44, s5, s44
	s_addc_u32 s45, s14, s45
	s_lshl_b32 s6, s6, 8
	s_add_i32 s46, s48, 16
	s_lshl_b32 s6, s6, s43
	s_ashr_i32 s47, s46, 31
	s_or_b32 s74, s6, s51
	s_lshl_b64 s[46:47], s[46:47], 20
	s_add_u32 s46, s5, s46
	s_addc_u32 s47, s14, s47
	s_add_i32 s48, s48, 32
	s_ashr_i32 s49, s48, 31
	s_lshl_b64 s[48:49], s[48:49], 20
	s_add_u32 s48, s5, s48
	s_addc_u32 s49, s14, s49
	s_add_i32 s6, s41, -2
	v_add_u32_e32 v2, s6, v211
	v_max_i32_e32 v2, 0, v2
	s_add_i32 s41, s85, -1
	v_min_u32_e32 v2, s41, v2
	v_lshl_or_b32 v2, v2, 5, v210
	v_lshlrev_b32_e32 v2, s43, v2
	v_add_u32_e32 v2, s51, v2
	v_mov_b32_e32 v3, v1
	v_lshlrev_b64 v[2:3], 7, v[2:3]
	v_or_b32_e32 v2, v2, v239
	v_lshl_add_u64 v[4:5], s[46:47], 0, v[2:3]
	v_lshl_add_u64 v[2:3], s[48:49], 0, v[2:3]
	global_load_dwordx4 v[110:113], v[4:5], off
	global_load_dwordx4 v[102:105], v[2:3], off
	v_add_u32_e32 v2, s6, v216
	v_max_i32_e32 v2, 0, v2
	v_min_u32_e32 v2, s41, v2
	v_lshl_or_b32 v2, v2, 5, v210
	v_lshlrev_b32_e32 v2, s43, v2
	v_add_u32_e32 v2, s51, v2
	v_mov_b32_e32 v3, v1
	v_lshlrev_b64 v[2:3], 7, v[2:3]
	v_or_b32_e32 v2, v2, v239
	v_lshl_add_u64 v[4:5], s[46:47], 0, v[2:3]
	v_lshl_add_u64 v[2:3], s[48:49], 0, v[2:3]
	global_load_dwordx4 v[106:109], v[4:5], off
	global_load_dwordx4 v[98:101], v[2:3], off
	v_add_u32_e32 v2, s6, v215
	v_max_i32_e32 v2, 0, v2
	v_min_u32_e32 v2, s41, v2
	v_lshl_or_b32 v2, v2, 5, v210
	v_lshlrev_b32_e32 v2, s43, v2
	v_add_u32_e32 v2, s51, v2
	v_mov_b32_e32 v3, v1
	v_lshlrev_b64 v[2:3], 7, v[2:3]
	v_or_b32_e32 v2, v2, v239
	v_lshl_add_u64 v[4:5], s[46:47], 0, v[2:3]
	v_lshl_add_u64 v[2:3], s[48:49], 0, v[2:3]
	global_load_dwordx4 v[94:97], v[4:5], off
	global_load_dwordx4 v[90:93], v[2:3], off
	v_add_u32_e32 v2, s6, v214
	v_max_i32_e32 v2, 0, v2
	v_min_u32_e32 v2, s41, v2
	v_lshl_or_b32 v2, v2, 5, v210
	v_lshlrev_b32_e32 v2, s43, v2
	v_add_u32_e32 v2, s51, v2
	v_mov_b32_e32 v3, v1
	v_lshlrev_b64 v[2:3], 7, v[2:3]
	v_or_b32_e32 v2, v2, v239
	v_lshl_add_u64 v[4:5], s[46:47], 0, v[2:3]
	v_lshl_add_u64 v[2:3], s[48:49], 0, v[2:3]
	global_load_dwordx4 v[86:89], v[4:5], off
	global_load_dwordx4 v[82:85], v[2:3], off
	v_add_u32_e32 v2, s6, v213
	v_max_i32_e32 v2, 0, v2
	v_min_u32_e32 v2, s41, v2
	v_lshl_or_b32 v2, v2, 5, v210
	v_lshlrev_b32_e32 v2, s43, v2
	v_add_u32_e32 v2, s51, v2
	v_mov_b32_e32 v3, v1
	v_lshlrev_b64 v[2:3], 7, v[2:3]
	v_or_b32_e32 v2, v2, v239
	v_lshl_add_u64 v[4:5], s[46:47], 0, v[2:3]
	v_lshl_add_u64 v[2:3], s[48:49], 0, v[2:3]
	global_load_dwordx4 v[78:81], v[4:5], off
	global_load_dwordx4 v[74:77], v[2:3], off
	v_add_u32_e32 v2, s6, v212
	v_max_i32_e32 v2, 0, v2
	v_min_u32_e32 v2, s41, v2
	v_lshl_or_b32 v2, v2, 5, v210
	v_lshlrev_b32_e32 v2, s43, v2
	v_add_u32_e32 v2, s51, v2
	v_mov_b32_e32 v3, v1
	v_lshlrev_b64 v[2:3], 7, v[2:3]
	v_or_b32_e32 v2, v2, v239
	v_lshl_add_u64 v[4:5], s[46:47], 0, v[2:3]
	v_lshl_add_u64 v[2:3], s[48:49], 0, v[2:3]
	global_load_dwordx4 v[70:73], v[4:5], off
	global_load_dwordx4 v[66:69], v[2:3], off
	v_lshlrev_b32_e32 v2, s43, v147
	v_add_u32_e32 v2, s74, v2
	v_ashrrev_i32_e32 v3, 31, v2
	v_lshlrev_b64 v[2:3], 7, v[2:3]
	v_lshl_add_u64 v[2:3], s[44:45], 0, v[2:3]
	v_lshl_add_u64 v[2:3], v[162:163], 1, v[2:3]
	global_load_dwordx4 v[114:117], v[2:3], off
	global_load_dwordx4 v[118:121], v[2:3], off offset:32
	global_load_dwordx4 v[122:125], v[2:3], off offset:64
	global_load_dwordx4 v[126:129], v[2:3], off offset:96
	s_ashr_i32 s41, s40, 31
	s_ashr_i32 s43, s42, 31
	s_lshl_b64 s[44:45], s[40:41], 24
	s_lshl_b64 s[46:47], s[42:43], 23
	s_lshl_b64 s[40:41], s[40:41], 19
	s_lshl_b64 s[42:43], s[42:43], 18
	s_add_u32 s44, s15, s44
	s_addc_u32 s45, s16, s45
	s_add_u32 s44, s44, s46
	s_addc_u32 s45, s45, s47
	s_lshl_b32 s46, s50, 7
	s_add_u32 s92, s44, s46
	s_addc_u32 s93, s45, 0
	s_add_u32 s40, s17, s40
	s_addc_u32 s41, s30, s41
	s_add_u32 s40, s40, s42
	s_addc_u32 s41, s41, s43
	s_lshl_b32 s42, s50, 2
	s_add_u32 s82, s40, s42
	s_addc_u32 s83, s41, 0

.LBB0_548:
	ds_read_b128 v[10:13], v244 offset:4096
	ds_read_b128 v[24:27], v245 offset:4096
	ds_read_b128 v[28:31], v246 offset:4096
	s_add_i32 s42, s4, 1
	s_cmp_gt_i32 s42, -1
	s_cselect_b64 s[40:41], -1, 0
	s_cmp_lt_i32 s42, s94
	s_cselect_b64 s[42:43], -1, 0
	s_and_b64 s[40:41], s[40:41], s[42:43]
	s_and_b64 vcc, exec, s[40:41]
	s_waitcnt lgkmcnt(2)
	v_mfma_f32_32x32x16_bf16 v[50:65], v[10:13], v[142:145], 0
	ds_read_b128 v[10:13], v247 offset:4096
	s_waitcnt lgkmcnt(2)
	v_mfma_f32_32x32x16_bf16 v[50:65], v[24:27], v[138:141], v[50:65]
	ds_read_b128 v[24:27], v244 offset:8192
	s_waitcnt lgkmcnt(2)
	v_mfma_f32_32x32x16_bf16 v[50:65], v[28:31], v[134:137], v[50:65]
	ds_read_b128 v[28:31], v245 offset:8192
	s_waitcnt lgkmcnt(2)
	v_mfma_f32_32x32x16_bf16 v[50:65], v[10:13], v[130:133], v[50:65]
	ds_read_b128 v[10:13], v246 offset:8192
	s_cbranch_vccnz .LBB0_550
	s_nop 10
	v_mov_b32_e32 v50, 0xf149f2ca
	v_mov_b32_e32 v51, v50
	v_mov_b32_e32 v52, v50
	v_mov_b32_e32 v53, v50
	v_mov_b32_e32 v54, v50
	v_mov_b32_e32 v55, v50
	v_mov_b32_e32 v56, v50
	v_mov_b32_e32 v57, v50
	v_mov_b32_e32 v58, v50
	v_mov_b32_e32 v59, v50
	v_mov_b32_e32 v60, v50
	v_mov_b32_e32 v61, v50
	v_mov_b32_e32 v62, v50
	v_mov_b32_e32 v63, v50
	v_mov_b32_e32 v64, v50
	v_mov_b32_e32 v65, v50
.LBB0_550:
	s_add_i32 s40, s4, 2
	s_cmp_lt_i32 s40, s94
	s_waitcnt lgkmcnt(2)
	v_mfma_f32_32x32x16_bf16 v[34:49], v[24:27], v[142:145], 0
	ds_read_b128 v[24:27], v247 offset:8192
	s_waitcnt lgkmcnt(2)
	v_mfma_f32_32x32x16_bf16 v[34:49], v[28:31], v[138:141], v[34:49]
	s_waitcnt lgkmcnt(1)
	v_mfma_f32_32x32x16_bf16 v[34:49], v[10:13], v[134:137], v[34:49]
	s_waitcnt lgkmcnt(0)
	v_mfma_f32_32x32x16_bf16 v[34:49], v[24:27], v[130:133], v[34:49]
	s_cbranch_scc1 .LBB0_552
	s_nop 10
	v_mov_b32_e32 v34, 0xf149f2ca
	v_mov_b32_e32 v35, v34
	v_mov_b32_e32 v36, v34
	v_mov_b32_e32 v37, v34
	v_mov_b32_e32 v38, v34
	v_mov_b32_e32 v39, v34
	v_mov_b32_e32 v40, v34
	v_mov_b32_e32 v41, v34
	v_mov_b32_e32 v42, v34
	v_mov_b32_e32 v43, v34
	v_mov_b32_e32 v44, v34
	v_mov_b32_e32 v45, v34
	v_mov_b32_e32 v46, v34
	v_mov_b32_e32 v47, v34
	v_mov_b32_e32 v48, v34
	v_mov_b32_e32 v49, v34
.LBB0_552:
	v_max3_f32 v10, v22, s97, v23
	v_max3_f32 v10, v10, v20, v21
	v_max3_f32 v10, v10, v18, v19
	v_max3_f32 v10, v10, v8, v9
	v_max3_f32 v10, v10, v6, v7
	v_max3_f32 v10, v10, v4, v5
	v_max3_f32 v10, v10, v2, v3
	v_max3_f32 v10, v10, v16, v17
	v_max3_f32 v10, v10, v50, v51
	v_max3_f32 v10, v10, v52, v53
	v_max3_f32 v10, v10, v54, v55
	v_max3_f32 v10, v10, v56, v57
	v_max3_f32 v10, v10, v58, v59
	v_max3_f32 v10, v10, v60, v61
	v_max3_f32 v10, v10, v62, v63
	v_max3_f32 v10, v10, v64, v65
	v_max3_f32 v10, v10, v34, v35
	v_max3_f32 v10, v10, v36, v37
	v_max3_f32 v10, v10, v38, v39
	v_max3_f32 v10, v10, v40, v41
	v_max3_f32 v10, v10, v42, v43
	v_max3_f32 v10, v10, v44, v45
	v_max3_f32 v10, v10, v46, v47
	v_max3_f32 v10, v10, v48, v49
	v_mov_b32_e32 v11, v10
	s_nop 1
	v_permlane32_swap_b32_e32 v10, v11
	v_max3_f32 v146, v10, v11, s97
	v_pk_add_f32 v[8:9], v[8:9], v[146:147] op_sel_hi:[1,0] neg_lo:[0,1] neg_hi:[0,1]
	v_pk_add_f32 v[6:7], v[6:7], v[146:147] op_sel_hi:[1,0] neg_lo:[0,1] neg_hi:[0,1]
	v_exp_f32_e32 v154, v8
	v_exp_f32_e32 v155, v9
	v_exp_f32_e32 v156, v6
	v_exp_f32_e32 v157, v7
	ds_read_b64_tr_b16 v[6:7], v220 offset:49152
	ds_read_b64_tr_b16 v[8:9], v220 offset:50176
	v_pk_add_f32 v[10:11], v[22:23], v[146:147] op_sel_hi:[1,0] neg_lo:[0,1] neg_hi:[0,1]
	v_pk_add_f32 v[4:5], v[4:5], v[146:147] op_sel_hi:[1,0] neg_lo:[0,1] neg_hi:[0,1]
	v_exp_f32_e32 v148, v10
	v_exp_f32_e32 v149, v11
	v_pk_add_f32 v[10:11], v[20:21], v[146:147] op_sel_hi:[1,0] neg_lo:[0,1] neg_hi:[0,1]
	v_pk_add_f32 v[2:3], v[2:3], v[146:147] op_sel_hi:[1,0] neg_lo:[0,1] neg_hi:[0,1]
	v_exp_f32_e32 v150, v10
	v_exp_f32_e32 v151, v11
	v_pk_add_f32 v[10:11], v[18:19], v[146:147] op_sel_hi:[1,0] neg_lo:[0,1] neg_hi:[0,1]
	v_exp_f32_e32 v158, v4
	v_exp_f32_e32 v152, v10
	v_exp_f32_e32 v153, v11
	v_exp_f32_e32 v159, v5
	v_exp_f32_e32 v160, v2
	v_exp_f32_e32 v161, v3
	v_cvt_pk_bf16_f32 v2, v148, v149
	v_cvt_pk_bf16_f32 v3, v150, v151
	v_cvt_pk_bf16_f32 v4, v152, v153
	v_cvt_pk_bf16_f32 v5, v154, v155
	ds_read_b64_tr_b16 v[10:11], v220 offset:51200
	ds_read_b64_tr_b16 v[12:13], v220 offset:52224
	ds_read_b64_tr_b16 v[166:167], v248
	ds_read_b64_tr_b16 v[168:169], v248 offset:1024
	ds_read_b64_tr_b16 v[174:175], v248 offset:2048
	ds_read_b64_tr_b16 v[176:177], v248 offset:3072
	s_waitcnt lgkmcnt(6)
	v_mfma_f32_32x32x16_bf16 v[18:33], v[6:9], v[2:5], 0
	v_add_f32_e64 v6, v16, -v146
	v_add_f32_e64 v7, v17, -v146
	v_cvt_pk_bf16_f32 v178, v156, v157
	v_exp_f32_e32 v164, v6
	v_exp_f32_e32 v165, v7
	v_cvt_pk_bf16_f32 v179, v158, v159
	v_cvt_pk_bf16_f32 v180, v160, v161
	v_pk_add_f32 v[50:51], v[50:51], v[146:147] op_sel_hi:[1,0] neg_lo:[0,1] neg_hi:[0,1]
	v_cvt_pk_bf16_f32 v181, v164, v165
	v_pk_add_f32 v[34:35], v[34:35], v[146:147] op_sel_hi:[1,0] neg_lo:[0,1] neg_hi:[0,1]
	s_add_i32 s40, s4, 3
	s_waitcnt lgkmcnt(4)
	v_mfma_f32_32x32x16_bf16 v[18:33], v[10:13], v[178:181], v[18:33]
	s_cmp_lt_i32 s40, s94
	s_waitcnt lgkmcnt(2)
	v_mfma_f32_32x32x16_bf16 v[2:17], v[166:169], v[2:5], 0
	v_exp_f32_e32 v166, v50
	v_exp_f32_e32 v167, v51
	v_pk_add_f32 v[50:51], v[52:53], v[146:147] op_sel_hi:[1,0] neg_lo:[0,1] neg_hi:[0,1]
	s_nop 0
	v_exp_f32_e32 v168, v50
	v_exp_f32_e32 v169, v51
	v_pk_add_f32 v[50:51], v[54:55], v[146:147] op_sel_hi:[1,0] neg_lo:[0,1] neg_hi:[0,1]
	s_waitcnt lgkmcnt(0)
	v_mfma_f32_32x32x16_bf16 v[2:17], v[174:177], v[178:181], v[2:17]
	v_exp_f32_e32 v170, v50
	v_exp_f32_e32 v171, v51
	v_pk_add_f32 v[50:51], v[56:57], v[146:147] op_sel_hi:[1,0] neg_lo:[0,1] neg_hi:[0,1]
	ds_read_b64_tr_b16 v[54:55], v220 offset:53248
	ds_read_b64_tr_b16 v[56:57], v220 offset:54272
	ds_read_b64_tr_b16 v[184:185], v248 offset:4096
	ds_read_b64_tr_b16 v[186:187], v248 offset:5120
	v_exp_f32_e32 v174, v50
	v_exp_f32_e32 v175, v51
	v_pk_add_f32 v[50:51], v[58:59], v[146:147] op_sel_hi:[1,0] neg_lo:[0,1] neg_hi:[0,1]
	v_cvt_pk_bf16_f32 v52, v170, v171
	v_exp_f32_e32 v176, v50
	v_exp_f32_e32 v177, v51
	v_pk_add_f32 v[50:51], v[60:61], v[146:147] op_sel_hi:[1,0] neg_lo:[0,1] neg_hi:[0,1]
	v_cvt_pk_bf16_f32 v53, v174, v175
	v_exp_f32_e32 v178, v50
	v_exp_f32_e32 v179, v51
	v_pk_add_f32 v[50:51], v[62:63], v[146:147] op_sel_hi:[1,0] neg_lo:[0,1] neg_hi:[0,1]
	ds_read_b64_tr_b16 v[58:59], v220 offset:55296
	v_exp_f32_e32 v180, v50
	v_exp_f32_e32 v181, v51
	v_cvt_pk_bf16_f32 v50, v166, v167
	v_cvt_pk_bf16_f32 v51, v168, v169
	ds_read_b64_tr_b16 v[60:61], v220 offset:56320
	ds_read_b64_tr_b16 v[196:197], v248 offset:6144
	ds_read_b64_tr_b16 v[198:199], v248 offset:7168
	s_waitcnt lgkmcnt(6)
	v_mfma_f32_32x32x16_bf16 v[18:33], v[54:57], v[50:53], v[18:33]
	v_add_f32_e64 v54, v64, -v146
	v_add_f32_e64 v55, v65, -v146
	v_cvt_pk_bf16_f32 v56, v180, v181
	v_exp_f32_e32 v182, v54
	v_exp_f32_e32 v183, v55
	v_cvt_pk_bf16_f32 v54, v176, v177
	v_cvt_pk_bf16_f32 v55, v178, v179
	v_cvt_pk_bf16_f32 v57, v182, v183
	s_waitcnt lgkmcnt(4)
	v_mfma_f32_32x32x16_bf16 v[2:17], v[184:187], v[50:53], v[2:17]
	v_exp_f32_e32 v184, v34
	v_exp_f32_e32 v185, v35
	v_pk_add_f32 v[34:35], v[36:37], v[146:147] op_sel_hi:[1,0] neg_lo:[0,1] neg_hi:[0,1]
	s_nop 0
	v_exp_f32_e32 v186, v34
	v_exp_f32_e32 v187, v35
	v_pk_add_f32 v[34:35], v[38:39], v[146:147] op_sel_hi:[1,0] neg_lo:[0,1] neg_hi:[0,1]
	s_waitcnt lgkmcnt(2)
	v_mfma_f32_32x32x16_bf16 v[18:33], v[58:61], v[54:57], v[18:33]
	v_exp_f32_e32 v188, v34
	v_exp_f32_e32 v189, v35
	v_pk_add_f32 v[34:35], v[40:41], v[146:147] op_sel_hi:[1,0] neg_lo:[0,1] neg_hi:[0,1]
	v_cvt_pk_bf16_f32 v36, v188, v189
	s_waitcnt lgkmcnt(0)
	v_mfma_f32_32x32x16_bf16 v[2:17], v[196:199], v[54:57], v[2:17]
	ds_read_b64_tr_b16 v[38:39], v220 offset:57344
	ds_read_b64_tr_b16 v[40:41], v220 offset:58368
	ds_read_b64_tr_b16 v[50:51], v248 offset:8192
	ds_read_b64_tr_b16 v[52:53], v248 offset:9216
	v_exp_f32_e32 v196, v34
	v_exp_f32_e32 v197, v35
	v_pk_add_f32 v[34:35], v[42:43], v[146:147] op_sel_hi:[1,0] neg_lo:[0,1] neg_hi:[0,1]
	ds_read_b64_tr_b16 v[42:43], v220 offset:59392
	v_exp_f32_e32 v198, v34
	v_exp_f32_e32 v199, v35
	v_pk_add_f32 v[34:35], v[44:45], v[146:147] op_sel_hi:[1,0] neg_lo:[0,1] neg_hi:[0,1]
	v_cvt_pk_bf16_f32 v37, v196, v197
	v_exp_f32_e32 v200, v34
	v_exp_f32_e32 v201, v35
	v_pk_add_f32 v[34:35], v[46:47], v[146:147] op_sel_hi:[1,0] neg_lo:[0,1] neg_hi:[0,1]
	ds_read_b64_tr_b16 v[44:45], v220 offset:60416
	v_exp_f32_e32 v202, v34
	v_exp_f32_e32 v203, v35
	v_cvt_pk_bf16_f32 v34, v184, v185
	v_cvt_pk_bf16_f32 v35, v186, v187
	ds_read_b64_tr_b16 v[54:55], v248 offset:10240
	ds_read_b64_tr_b16 v[56:57], v248 offset:11264
	s_waitcnt lgkmcnt(6)
	v_mfma_f32_32x32x16_bf16 v[18:33], v[38:41], v[34:37], v[18:33]
	v_add_f32_e64 v38, v48, -v146
	v_add_f32_e64 v39, v49, -v146
	v_cvt_pk_bf16_f32 v40, v202, v203
	v_exp_f32_e32 v204, v38
	v_exp_f32_e32 v205, v39
	v_cvt_pk_bf16_f32 v38, v198, v199
	v_cvt_pk_bf16_f32 v39, v200, v201
	v_cvt_pk_bf16_f32 v41, v204, v205
	s_waitcnt lgkmcnt(4)
	v_mfma_f32_32x32x16_bf16 v[2:17], v[50:53], v[34:37], v[2:17]
	ds_read_b128 v[34:37], v244 offset:12288
	ds_read_b128 v[50:53], v245 offset:12288
	ds_read_b128 v[58:61], v246 offset:12288
	ds_read_b128 v[62:65], v247 offset:12288
	s_waitcnt lgkmcnt(6)
	v_mfma_f32_32x32x16_bf16 v[18:33], v[42:45], v[38:41], v[18:33]
	s_waitcnt lgkmcnt(4)
	v_mfma_f32_32x32x16_bf16 v[2:17], v[54:57], v[38:41], v[2:17]
	s_waitcnt lgkmcnt(3)
	v_mfma_f32_32x32x16_bf16 v[34:49], v[34:37], v[142:145], 0
	s_waitcnt lgkmcnt(2)
	v_mfma_f32_32x32x16_bf16 v[34:49], v[50:53], v[138:141], v[34:49]
	ds_read_b128 v[50:53], v244 offset:16384
	s_waitcnt lgkmcnt(2)
	v_mfma_f32_32x32x16_bf16 v[34:49], v[58:61], v[134:137], v[34:49]
	s_waitcnt lgkmcnt(1)
	v_mfma_f32_32x32x16_bf16 v[34:49], v[62:65], v[130:133], v[34:49]
	s_cbranch_scc1 .LBB0_554
	s_nop 10
	v_mov_b32_e32 v34, 0xf149f2ca
	v_mov_b32_e32 v35, v34
	v_mov_b32_e32 v36, v34
	v_mov_b32_e32 v37, v34
	v_mov_b32_e32 v38, v34
	v_mov_b32_e32 v39, v34
	v_mov_b32_e32 v40, v34
	v_mov_b32_e32 v41, v34
	v_mov_b32_e32 v42, v34
	v_mov_b32_e32 v43, v34
	v_mov_b32_e32 v44, v34
	v_mov_b32_e32 v45, v34
	v_mov_b32_e32 v46, v34
	v_mov_b32_e32 v47, v34
	v_mov_b32_e32 v48, v34
	v_mov_b32_e32 v49, v34
.LBB0_554:
	s_add_i32 s4, s4, 4
	v_cmp_lt_i32_e32 vcc, 26, v249
	v_cmp_lt_i32_e64 s[40:41], -1, v249
	v_cmp_lt_i32_e64 s[42:43], 0, v249
	v_cmp_lt_i32_e64 s[44:45], 1, v249
	v_cmp_lt_i32_e64 s[46:47], 2, v249
	v_cmp_lt_i32_e64 s[48:49], 7, v249
	v_cmp_lt_i32_e64 s[50:51], 8, v249
	s_waitcnt lgkmcnt(0)
	v_mfma_f32_32x32x16_bf16 v[50:65], v[50:53], v[142:145], 0
	ds_read_b128 v[142:145], v245 offset:16384
	v_cmp_lt_i32_e64 s[52:53], 9, v249
	v_cmp_lt_i32_e64 s[54:55], 10, v249
	v_cmp_lt_i32_e64 s[56:57], 15, v249
	v_cmp_lt_i32_e64 s[58:59], 16, v249
	v_cmp_lt_i32_e64 s[60:61], 17, v249
	v_cmp_lt_i32_e64 s[62:63], 18, v249
	v_cmp_lt_i32_e64 s[64:65], 23, v249
	s_waitcnt lgkmcnt(0)
	v_mfma_f32_32x32x16_bf16 v[50:65], v[142:145], v[138:141], v[50:65]
	ds_read_b128 v[138:141], v246 offset:16384
	ds_read_b128 v[142:145], v247 offset:16384
	v_cmp_lt_i32_e64 s[66:67], 24, v249
	s_cmp_lt_i32 s4, s94
	v_cmp_lt_i32_e64 s[68:69], 25, v249
	s_waitcnt lgkmcnt(1)
	v_mfma_f32_32x32x16_bf16 v[50:65], v[138:141], v[134:137], v[50:65]
	s_waitcnt lgkmcnt(0)
	v_mfma_f32_32x32x16_bf16 v[50:65], v[142:145], v[130:133], v[50:65]
	s_cbranch_scc1 .LBB0_556
	v_mov_b32_e32 v136, 0xf149f2ca
	v_mov_b32_e32 v137, v136
	v_mov_b32_e32 v134, v136
	v_mov_b32_e32 v135, v136
	v_mov_b32_e32 v132, v136
	v_mov_b32_e32 v133, v136
	v_mov_b32_e32 v130, v136
	v_mov_b32_e32 v131, v136
	s_nop 2
	v_mov_b32_e32 v56, v136
	v_mov_b32_e32 v57, v136
	v_mov_b32_e32 v54, v136
	v_mov_b32_e32 v55, v136
	v_mov_b32_e32 v52, v136
	v_mov_b32_e32 v53, v136
	v_mov_b32_e32 v64, v136
	v_mov_b32_e32 v65, v136
	s_branch .LBB0_557

.LBB0_597:
	s_or_b64 exec, exec, s[26:27]
	global_load_dwordx4 v[128:131], v[34:35], off
	global_load_dwordx4 v[132:135], v[36:37], off
	global_load_dwordx4 v[136:139], v[38:39], off
	global_load_dwordx4 v[140:143], v[40:41], off
	s_movk_i32 s4, 0x2000
	v_cmp_gt_u32_e32 vcc, s4, v22
	s_waitcnt vmcnt(4)
	ds_write_b128 v99, v[18:21]
	s_mov_b64 s[26:27], -1
	v_cndmask_b32_e32 v9, 0, v9, vcc
	v_cndmask_b32_e32 v8, 0, v8, vcc
	v_cndmask_b32_e32 v7, 0, v7, vcc
	v_cndmask_b32_e32 v6, 0, v6, vcc
	v_cmp_gt_u32_e32 vcc, s4, v23
	ds_write_b128 v100, v[6:9]
	s_nop 0
	v_cndmask_b32_e32 v5, 0, v5, vcc
	v_cndmask_b32_e32 v4, 0, v4, vcc
	v_cndmask_b32_e32 v3, 0, v3, vcc
	v_cndmask_b32_e32 v2, 0, v2, vcc
	v_cmp_gt_u32_e32 vcc, s4, v24
	ds_write_b128 v101, v[2:5]
	s_nop 0
	v_cndmask_b32_e32 v5, 0, v17, vcc
	v_cndmask_b32_e32 v4, 0, v16, vcc
	v_cndmask_b32_e32 v3, 0, v15, vcc
	v_cndmask_b32_e32 v2, 0, v14, vcc
	v_cmp_gt_u32_e32 vcc, s4, v25
	ds_write_b128 v102, v[2:5]
	v_readlane_b32 s4, v253, 26
	v_cndmask_b32_e32 v5, 0, v13, vcc
	v_cndmask_b32_e32 v4, 0, v12, vcc
	v_cndmask_b32_e32 v3, 0, v11, vcc
	v_cndmask_b32_e32 v2, 0, v10, vcc
	ds_write_b128 v103, v[2:5]
	s_cmp_lt_i32 s4, 2
	s_waitcnt vmcnt(3)
	ds_write_b128 v104, v[128:131]
	s_waitcnt vmcnt(2)
	ds_write_b128 v105, v[132:135]
	s_waitcnt vmcnt(1)
	ds_write_b128 v106, v[136:139]
	s_waitcnt vmcnt(0)
	ds_write_b128 v107, v[140:143]
	s_waitcnt lgkmcnt(0)
	s_barrier
	s_cbranch_scc1 .LBB0_603
	v_readlane_b32 s4, v253, 26
	s_cmp_gt_i32 s4, 2
	s_cbranch_scc0 .LBB0_600
	v_mov_b32_e32 v123, v1
	ds_read_u16_d16_hi v123, v55 offset:0
	v_mov_b32_e32 v124, v1
	ds_read_u16_d16_hi v124, v55 offset:0x200
	v_mov_b32_e32 v125, v1
	ds_read_u16_d16_hi v125, v55 offset:0x400
	v_mov_b32_e32 v126, v1
	ds_read_u16_d16_hi v126, v55 offset:0x600
	v_mov_b32_e32 v127, v1
	ds_read_u16_d16_hi v127, v55 offset:0x800
	v_mov_b32_e32 v122, v1
	ds_read_u16_d16_hi v122, v55 offset:0xa00
	v_mov_b32_e32 v121, v1
	ds_read_u16_d16_hi v121, v55 offset:0xc00
	v_mov_b32_e32 v120, v1
	ds_read_u16_d16_hi v120, v55 offset:0xe00
	v_mov_b32_e32 v119, v1
	ds_read_u16_d16_hi v119, v55 offset:0x1000
	v_mov_b32_e32 v118, v1
	ds_read_u16_d16_hi v118, v55 offset:0x1200
	v_mov_b32_e32 v117, v1
	ds_read_u16_d16_hi v117, v55 offset:0x1400
	v_mov_b32_e32 v116, v1
	ds_read_u16_d16_hi v116, v55 offset:0x1600
	v_mov_b32_e32 v115, v1
	ds_read_u16_d16_hi v115, v55 offset:0x1800
	v_mov_b32_e32 v114, v1
	ds_read_u16_d16_hi v114, v55 offset:0x1a00
	v_mov_b32_e32 v113, v1
	ds_read_u16_d16_hi v113, v55 offset:0x1c00
	v_mov_b32_e32 v33, v1
	ds_read_u16_d16_hi v33, v55 offset:0x1e00
	v_mov_b32_e32 v32, v1
	ds_read_u16_d16_hi v32, v55 offset:0x2000
	v_mov_b32_e32 v31, v1
	ds_read_u16_d16_hi v31, v55 offset:0x2200
	v_mov_b32_e32 v30, v1
	ds_read_u16_d16_hi v30, v55 offset:0x2400
	v_mov_b32_e32 v29, v1
	ds_read_u16_d16_hi v29, v55 offset:0x2600
	v_mov_b32_e32 v28, v1
	ds_read_u16_d16_hi v28, v55 offset:0x2800
	v_mov_b32_e32 v27, v1
	ds_read_u16_d16_hi v27, v55 offset:0x2a00
	v_mov_b32_e32 v26, v1
	ds_read_u16_d16_hi v26, v55 offset:0x2c00
	v_mov_b32_e32 v24, v1
	ds_read_u16_d16_hi v24, v55 offset:0x2e00
	v_mov_b32_e32 v21, v1
	ds_read_u16_d16_hi v21, v55 offset:0x3000
	v_mov_b32_e32 v18, v1
	ds_read_u16_d16_hi v18, v55 offset:0x3200
	v_mov_b32_e32 v15, v1
	ds_read_u16_d16_hi v15, v55 offset:0x3400
	v_mov_b32_e32 v12, v1
	ds_read_u16_d16_hi v12, v55 offset:0x3600
	v_mov_b32_e32 v9, v1
	ds_read_u16_d16_hi v9, v55 offset:0x3800
	v_mov_b32_e32 v6, v1
	ds_read_u16_d16_hi v6, v55 offset:0x3a00
	v_mov_b32_e32 v3, v1
	ds_read_u16_d16_hi v3, v55 offset:0x3c00
	v_mov_b32_e32 v25, v1
	ds_read_u16_d16_hi v25, v55 offset:0x3e00
	v_mov_b32_e32 v22, v1
	ds_read_u16_d16_hi v22, v55 offset:0x4000
	v_mov_b32_e32 v19, v1
	ds_read_u16_d16_hi v19, v55 offset:0x4200
	v_mov_b32_e32 v16, v1
	ds_read_u16_d16_hi v16, v55 offset:0x4400
	v_mov_b32_e32 v13, v1
	ds_read_u16_d16_hi v13, v55 offset:0x4600
	v_mov_b32_e32 v10, v1
	ds_read_u16_d16_hi v10, v55 offset:0x4800
	v_mov_b32_e32 v7, v1
	ds_read_u16_d16_hi v7, v55 offset:0x4a00
	v_mov_b32_e32 v4, v1
	ds_read_u16_d16_hi v4, v55 offset:0x4c00
	v_mov_b32_e32 v2, v1
	ds_read_u16_d16_hi v2, v55 offset:0x4e00
	v_mov_b32_e32 v23, v1
	ds_read_u16_d16_hi v23, v55 offset:0x5000
	v_mov_b32_e32 v20, v1
	ds_read_u16_d16_hi v20, v55 offset:0x5200
	v_mov_b32_e32 v17, v1
	ds_read_u16_d16_hi v17, v55 offset:0x5400
	v_mov_b32_e32 v14, v1
	ds_read_u16_d16_hi v14, v55 offset:0x5600
	v_mov_b32_e32 v11, v1
	ds_read_u16_d16_hi v11, v55 offset:0x5800
	v_mov_b32_e32 v8, v1
	ds_read_u16_d16_hi v8, v55 offset:0x5a00
	v_mov_b32_e32 v5, v1
	ds_read_u16_d16_hi v5, v55 offset:0x5c00
	s_waitcnt lgkmcnt(0)
	v_add_u32_e32 v129, s14, v53
	v_add_f32_e32 v128, 0, v123
	v_add_f32_e32 v128, v128, v124
	v_add_f32_e32 v128, v128, v125
	v_add_f32_e32 v128, v128, v126
	v_add_f32_e32 v128, v128, v127
	v_max_i32_e32 v130, 8, v129
	v_add_f32_e32 v128, v128, v122
	v_min_i32_e32 v129, 0x1ff8, v129
	v_sub_u32_e32 v129, v129, v130
	v_add_f32_e32 v128, v128, v121
	v_add_u32_e32 v129, 16, v129
	v_add_f32_e32 v128, v128, v120
	v_cvt_f32_i32_e32 v129, v129
	v_add_f32_e32 v128, v128, v119
	v_rcp_iflag_f32_e32 v129, v129
	v_add_f32_e32 v128, v128, v118
	v_add_f32_e32 v128, v128, v117
	v_add_f32_e32 v128, v128, v116
	v_add_f32_e32 v128, v128, v115
	v_add_u32_e32 v130, v54, v56
	v_add_f32_e32 v128, v128, v114
	v_add_f32_e32 v128, v128, v113
	v_add_f32_e32 v128, v128, v33
	v_fma_f32 v129, v129, v128, -v119
	v_sub_f32_e32 v123, v32, v123
	v_cvt_pk_bf16_f32 v129, v129, s0
	v_add_f32_e32 v123, v128, v123
	v_add_u32_e32 v128, s14, v57
	ds_write_b16 v130, v129 offset:40960
	v_max_i32_e32 v129, 8, v128
	v_min_i32_e32 v128, 0x1ff8, v128
	v_sub_u32_e32 v128, v128, v129
	v_add_u32_e32 v128, 16, v128
	v_cvt_f32_i32_e32 v128, v128
	v_sub_f32_e32 v124, v31, v124
	v_sub_f32_e32 v122, v27, v122
	v_sub_f32_e32 v121, v26, v121
	v_rcp_iflag_f32_e32 v128, v128
	v_sub_f32_e32 v120, v24, v120
	v_sub_f32_e32 v119, v21, v119
	s_mov_b64 s[26:27], 0
	v_fma_f32 v128, v128, v123, -v118
	v_cvt_pk_bf16_f32 v128, v128, s0
	v_add_f32_e32 v123, v123, v124
	v_add_u32_e32 v124, s14, v58
	ds_write_b16 v130, v128 offset:41488
	v_max_i32_e32 v128, 8, v124
	v_min_i32_e32 v124, 0x1ff8, v124
	v_sub_u32_e32 v124, v124, v128
	v_add_u32_e32 v124, 16, v124
	v_cvt_f32_i32_e32 v124, v124
	v_sub_f32_e32 v118, v18, v118
	v_rcp_iflag_f32_e32 v124, v124
	s_nop 0
	v_fma_f32 v124, v124, v123, -v117
	v_cvt_pk_bf16_f32 v124, v124, s0
	ds_write_b16 v130, v124 offset:42016
	v_sub_f32_e32 v124, v30, v125
	v_add_f32_e32 v123, v123, v124
	v_add_u32_e32 v124, s14, v59
	v_max_i32_e32 v125, 8, v124
	v_min_i32_e32 v124, 0x1ff8, v124
	v_sub_u32_e32 v124, v124, v125
	v_add_u32_e32 v124, 16, v124
	v_cvt_f32_i32_e32 v124, v124
	v_sub_f32_e32 v117, v15, v117
	v_rcp_iflag_f32_e32 v124, v124
	s_nop 0
	v_fma_f32 v124, v124, v123, -v116
	v_cvt_pk_bf16_f32 v124, v124, s0
	ds_write_b16 v130, v124 offset:42544
	v_sub_f32_e32 v124, v29, v126
	v_add_f32_e32 v123, v123, v124
	v_add_u32_e32 v124, s14, v60
	v_max_i32_e32 v125, 8, v124
	v_min_i32_e32 v124, 0x1ff8, v124
	v_sub_u32_e32 v124, v124, v125
	v_add_u32_e32 v124, 16, v124
	v_cvt_f32_i32_e32 v124, v124
	v_sub_f32_e32 v116, v12, v116
	v_rcp_iflag_f32_e32 v124, v124
	s_nop 0
	v_fma_f32 v124, v124, v123, -v115
	v_cvt_pk_bf16_f32 v124, v124, s0
	ds_write_b16 v130, v124 offset:43072
	v_sub_f32_e32 v124, v28, v127
	v_add_f32_e32 v123, v123, v124
	v_add_u32_e32 v124, s14, v61
	v_max_i32_e32 v125, 8, v124
	v_min_i32_e32 v124, 0x1ff8, v124
	v_sub_u32_e32 v124, v124, v125
	v_add_u32_e32 v124, 16, v124
	v_cvt_f32_i32_e32 v124, v124
	v_add_u32_e32 v125, v54, v62
	v_add_f32_e32 v122, v123, v122
	v_add_f32_e32 v121, v122, v121
	v_rcp_iflag_f32_e32 v124, v124
	v_add_f32_e32 v120, v121, v120
	v_add_f32_e32 v119, v120, v119
	v_add_f32_e32 v118, v119, v118
	v_fma_f32 v124, v124, v123, -v114
	v_cvt_pk_bf16_f32 v124, v124, s0
	v_add_u32_e32 v123, s14, v63
	ds_write_b16 v125, v124 offset:40960
	v_max_i32_e32 v124, 8, v123
	v_min_i32_e32 v123, 0x1ff8, v123
	v_sub_u32_e32 v123, v123, v124
	v_add_u32_e32 v123, 16, v123
	v_cvt_f32_i32_e32 v123, v123
	v_add_f32_e32 v117, v118, v117
	v_add_f32_e32 v116, v117, v116
	v_sub_f32_e32 v115, v9, v115
	v_rcp_iflag_f32_e32 v123, v123
	v_add_f32_e32 v115, v116, v115
	v_sub_f32_e32 v114, v6, v114
	v_add_f32_e32 v114, v115, v114
	v_fma_f32 v123, v123, v122, -v113
	v_cvt_pk_bf16_f32 v123, v123, s0
	v_add_u32_e32 v122, s14, v64
	ds_write_b16 v125, v123 offset:41488
	v_max_i32_e32 v123, 8, v122
	v_min_i32_e32 v122, 0x1ff8, v122
	v_sub_u32_e32 v122, v122, v123
	v_add_u32_e32 v122, 16, v122
	v_cvt_f32_i32_e32 v122, v122
	v_sub_f32_e32 v113, v3, v113
	v_add_f32_e32 v113, v114, v113
	v_rcp_iflag_f32_e32 v122, v122
	s_nop 0
	v_fma_f32 v122, v122, v121, -v33
	v_cvt_pk_bf16_f32 v122, v122, s0
	v_add_u32_e32 v121, s14, v65
	ds_write_b16 v125, v122 offset:42016
	v_max_i32_e32 v122, 8, v121
	v_min_i32_e32 v121, 0x1ff8, v121
	v_sub_u32_e32 v121, v121, v122
	v_add_u32_e32 v121, 16, v121
	v_cvt_f32_i32_e32 v121, v121
	v_sub_f32_e32 v33, v25, v33
	v_add_f32_e32 v33, v113, v33
	v_rcp_iflag_f32_e32 v121, v121
	s_nop 0
	v_fma_f32 v121, v121, v120, -v32
	v_cvt_pk_bf16_f32 v121, v121, s0
	v_add_u32_e32 v120, s14, v66
	ds_write_b16 v125, v121 offset:42544
	v_max_i32_e32 v121, 8, v120
	v_min_i32_e32 v120, 0x1ff8, v120
	v_sub_u32_e32 v120, v120, v121
	v_add_u32_e32 v120, 16, v120
	v_cvt_f32_i32_e32 v120, v120
	v_sub_f32_e32 v32, v22, v32
	v_add_f32_e32 v32, v33, v32
	v_rcp_iflag_f32_e32 v120, v120
	s_nop 0
	v_fma_f32 v120, v120, v119, -v31
	v_cvt_pk_bf16_f32 v120, v120, s0
	v_add_u32_e32 v119, s14, v67
	ds_write_b16 v125, v120 offset:43072
	v_max_i32_e32 v120, 8, v119
	v_min_i32_e32 v119, 0x1ff8, v119
	v_sub_u32_e32 v119, v119, v120
	v_add_u32_e32 v119, 16, v119
	v_cvt_f32_i32_e32 v119, v119
	v_add_u32_e32 v120, v54, v68
	v_sub_f32_e32 v31, v19, v31
	v_add_f32_e32 v31, v32, v31
	v_rcp_iflag_f32_e32 v119, v119
	s_nop 0
	v_fma_f32 v119, v119, v118, -v30
	v_cvt_pk_bf16_f32 v119, v119, s0
	v_add_u32_e32 v118, s14, v69
	ds_write_b16 v120, v119 offset:40960
	v_max_i32_e32 v119, 8, v118
	v_min_i32_e32 v118, 0x1ff8, v118
	v_sub_u32_e32 v118, v118, v119
	v_add_u32_e32 v118, 16, v118
	v_cvt_f32_i32_e32 v118, v118
	v_sub_f32_e32 v30, v16, v30
	v_add_f32_e32 v30, v31, v30
	v_rcp_iflag_f32_e32 v118, v118
	s_nop 0
	v_fma_f32 v118, v118, v117, -v29
	v_cvt_pk_bf16_f32 v118, v118, s0
	v_add_u32_e32 v117, s14, v70
	ds_write_b16 v120, v118 offset:41488
	v_max_i32_e32 v118, 8, v117
	v_min_i32_e32 v117, 0x1ff8, v117
	v_sub_u32_e32 v117, v117, v118
	v_add_u32_e32 v117, 16, v117
	v_cvt_f32_i32_e32 v117, v117
	v_sub_f32_e32 v29, v13, v29
	v_add_f32_e32 v29, v30, v29
	v_rcp_iflag_f32_e32 v117, v117
	s_nop 0
	v_fma_f32 v117, v117, v116, -v28
	v_cvt_pk_bf16_f32 v117, v117, s0
	v_add_u32_e32 v116, s14, v71
	ds_write_b16 v120, v117 offset:42016
	v_max_i32_e32 v117, 8, v116
	v_min_i32_e32 v116, 0x1ff8, v116
	v_sub_u32_e32 v116, v116, v117
	v_add_u32_e32 v116, 16, v116
	v_cvt_f32_i32_e32 v116, v116
	v_sub_f32_e32 v28, v10, v28
	v_add_f32_e32 v28, v29, v28
	v_rcp_iflag_f32_e32 v116, v116
	s_nop 0
	v_fma_f32 v116, v116, v115, -v27
	v_cvt_pk_bf16_f32 v116, v116, s0
	v_add_u32_e32 v115, s14, v72
	ds_write_b16 v120, v116 offset:42544
	v_max_i32_e32 v116, 8, v115
	v_min_i32_e32 v115, 0x1ff8, v115
	v_sub_u32_e32 v115, v115, v116
	v_add_u32_e32 v115, 16, v115
	v_cvt_f32_i32_e32 v115, v115
	v_sub_f32_e32 v27, v7, v27
	v_add_f32_e32 v27, v28, v27
	v_rcp_iflag_f32_e32 v115, v115
	s_nop 0
	v_fma_f32 v115, v115, v114, -v26
	v_cvt_pk_bf16_f32 v115, v115, s0
	v_add_u32_e32 v114, s14, v73
	ds_write_b16 v120, v115 offset:43072
	v_max_i32_e32 v115, 8, v114
	v_min_i32_e32 v114, 0x1ff8, v114
	v_sub_u32_e32 v114, v114, v115
	v_add_u32_e32 v114, 16, v114
	v_cvt_f32_i32_e32 v114, v114
	v_add_u32_e32 v115, v54, v74
	v_sub_f32_e32 v26, v4, v26
	v_add_f32_e32 v26, v27, v26
	v_rcp_iflag_f32_e32 v114, v114
	s_nop 0
	v_fma_f32 v114, v114, v113, -v24
	v_cvt_pk_bf16_f32 v114, v114, s0
	v_add_u32_e32 v113, s14, v75
	ds_write_b16 v115, v114 offset:40960
	v_max_i32_e32 v114, 8, v113
	v_min_i32_e32 v113, 0x1ff8, v113
	v_sub_u32_e32 v113, v113, v114
	v_add_u32_e32 v113, 16, v113
	v_cvt_f32_i32_e32 v113, v113
	v_sub_f32_e32 v24, v2, v24
	v_add_f32_e32 v24, v26, v24
	v_rcp_iflag_f32_e32 v113, v113
	s_nop 0
	v_fma_f32 v113, v113, v33, -v21
	v_cvt_pk_bf16_f32 v113, v113, s0
	v_add_u32_e32 v33, s14, v76
	ds_write_b16 v115, v113 offset:41488
	v_max_i32_e32 v113, 8, v33
	v_min_i32_e32 v33, 0x1ff8, v33
	v_sub_u32_e32 v33, v33, v113
	v_add_u32_e32 v33, 16, v33
	v_cvt_f32_i32_e32 v33, v33
	v_sub_f32_e32 v21, v23, v21
	v_add_f32_e32 v21, v24, v21
	v_rcp_iflag_f32_e32 v33, v33
	s_nop 0
	v_fma_f32 v33, v33, v32, -v18
	v_cvt_pk_bf16_f32 v33, v33, s0
	v_add_u32_e32 v32, s14, v77
	ds_write_b16 v115, v33 offset:42016
	v_max_i32_e32 v33, 8, v32
	v_min_i32_e32 v32, 0x1ff8, v32
	v_sub_u32_e32 v32, v32, v33
	v_add_u32_e32 v32, 16, v32
	v_cvt_f32_i32_e32 v32, v32
	v_sub_f32_e32 v18, v20, v18
	v_add_f32_e32 v18, v21, v18
	v_rcp_iflag_f32_e32 v32, v32
	s_nop 0
	v_fma_f32 v32, v32, v31, -v15
	v_cvt_pk_bf16_f32 v32, v32, s0
	v_add_u32_e32 v31, s14, v78
	ds_write_b16 v115, v32 offset:42544
	v_max_i32_e32 v32, 8, v31
	v_min_i32_e32 v31, 0x1ff8, v31
	v_sub_u32_e32 v31, v31, v32
	v_add_u32_e32 v31, 16, v31
	v_cvt_f32_i32_e32 v31, v31
	v_sub_f32_e32 v15, v17, v15
	v_add_f32_e32 v15, v18, v15
	v_rcp_iflag_f32_e32 v31, v31
	s_nop 0
	v_fma_f32 v31, v31, v30, -v12
	v_cvt_pk_bf16_f32 v31, v31, s0
	v_add_u32_e32 v30, s14, v79
	ds_write_b16 v115, v31 offset:43072
	v_max_i32_e32 v31, 8, v30
	v_min_i32_e32 v30, 0x1ff8, v30
	v_sub_u32_e32 v30, v30, v31
	v_add_u32_e32 v30, 16, v30
	v_cvt_f32_i32_e32 v30, v30
	v_add_u32_e32 v31, v54, v80
	v_sub_f32_e32 v12, v14, v12
	v_add_f32_e32 v12, v15, v12
	v_rcp_iflag_f32_e32 v30, v30
	s_nop 0
	v_fma_f32 v30, v30, v29, -v9
	v_cvt_pk_bf16_f32 v30, v30, s0
	v_add_u32_e32 v29, s14, v81
	ds_write_b16 v31, v30 offset:40960
	v_max_i32_e32 v30, 8, v29
	v_min_i32_e32 v29, 0x1ff8, v29
	v_sub_u32_e32 v29, v29, v30
	v_add_u32_e32 v29, 16, v29
	v_cvt_f32_i32_e32 v29, v29
	v_sub_f32_e32 v9, v11, v9
	v_add_f32_e32 v9, v12, v9
	v_rcp_iflag_f32_e32 v29, v29
	s_nop 0
	v_fma_f32 v29, v29, v28, -v6
	v_cvt_pk_bf16_f32 v29, v29, s0
	v_add_u32_e32 v28, s14, v82
	ds_write_b16 v31, v29 offset:41488
	v_max_i32_e32 v29, 8, v28
	v_min_i32_e32 v28, 0x1ff8, v28
	v_sub_u32_e32 v28, v28, v29
	v_add_u32_e32 v28, 16, v28
	v_cvt_f32_i32_e32 v28, v28
	v_sub_f32_e32 v6, v8, v6
	v_add_f32_e32 v6, v9, v6
	v_rcp_iflag_f32_e32 v28, v28
	s_nop 0
	v_fma_f32 v28, v28, v27, -v3
	v_cvt_pk_bf16_f32 v28, v28, s0
	v_add_u32_e32 v27, s14, v83
	ds_write_b16 v31, v28 offset:42016
	v_max_i32_e32 v28, 8, v27
	v_min_i32_e32 v27, 0x1ff8, v27
	v_sub_u32_e32 v27, v27, v28
	v_add_u32_e32 v27, 16, v27
	v_cvt_f32_i32_e32 v27, v27
	v_sub_f32_e32 v3, v5, v3
	v_add_f32_e32 v119, v6, v3
	v_add_u32_e32 v3, s14, v91
	v_rcp_iflag_f32_e32 v27, v27
	s_nop 0
	v_fma_f32 v25, v27, v26, -v25
	v_cvt_pk_bf16_f32 v25, v25, s0
	ds_write_b16 v31, v25 offset:42544
	v_add_u32_e32 v25, s14, v84
	v_max_i32_e32 v26, 8, v25
	v_min_i32_e32 v25, 0x1ff8, v25
	v_sub_u32_e32 v25, v25, v26
	v_add_u32_e32 v25, 16, v25
	v_cvt_f32_i32_e32 v25, v25
	v_rcp_iflag_f32_e32 v25, v25
	s_nop 0
	v_fma_f32 v22, v25, v24, -v22
	v_cvt_pk_bf16_f32 v22, v22, s0
	ds_write_b16 v31, v22 offset:43072
	v_add_u32_e32 v22, s14, v85
	v_max_i32_e32 v23, 8, v22
	v_min_i32_e32 v22, 0x1ff8, v22
	v_sub_u32_e32 v22, v22, v23
	v_add_u32_e32 v22, 16, v22
	v_cvt_f32_i32_e32 v22, v22
	v_rcp_iflag_f32_e32 v22, v22
	s_nop 0
	v_fma_f32 v19, v22, v21, -v19
	v_cvt_pk_bf16_f32 v19, v19, s0
	ds_write_b16 v31, v19 offset:43600
	v_add_u32_e32 v19, s14, v86
	v_max_i32_e32 v20, 8, v19
	v_min_i32_e32 v19, 0x1ff8, v19
	v_sub_u32_e32 v19, v19, v20
	v_add_u32_e32 v19, 16, v19
	v_cvt_f32_i32_e32 v19, v19
	v_rcp_iflag_f32_e32 v19, v19
	s_nop 0
	v_fma_f32 v16, v19, v18, -v16
	v_cvt_pk_bf16_f32 v16, v16, s0
	ds_write_b16 v31, v16 offset:44128
	v_add_u32_e32 v16, s14, v87
	v_max_i32_e32 v17, 8, v16
	v_min_i32_e32 v16, 0x1ff8, v16
	v_sub_u32_e32 v16, v16, v17
	v_add_u32_e32 v16, 16, v16
	v_cvt_f32_i32_e32 v16, v16
	v_rcp_iflag_f32_e32 v16, v16
	s_nop 0
	v_fma_f32 v13, v16, v15, -v13
	v_cvt_pk_bf16_f32 v13, v13, s0
	ds_write_b16 v31, v13 offset:44656
	v_add_u32_e32 v13, s14, v88
	v_max_i32_e32 v14, 8, v13
	v_min_i32_e32 v13, 0x1ff8, v13
	v_sub_u32_e32 v13, v13, v14
	v_add_u32_e32 v13, 16, v13
	v_cvt_f32_i32_e32 v13, v13
	v_rcp_iflag_f32_e32 v13, v13
	s_nop 0
	v_fma_f32 v10, v13, v12, -v10
	v_cvt_pk_bf16_f32 v10, v10, s0
	ds_write_b16 v31, v10 offset:45184
	v_add_u32_e32 v10, s14, v89
	v_max_i32_e32 v11, 8, v10
	v_min_i32_e32 v10, 0x1ff8, v10
	v_sub_u32_e32 v10, v10, v11
	v_add_u32_e32 v10, 16, v10
	v_cvt_f32_i32_e32 v10, v10
	v_rcp_iflag_f32_e32 v10, v10
	s_nop 0
	v_fma_f32 v7, v10, v9, -v7
	v_cvt_pk_bf16_f32 v7, v7, s0
	ds_write_b16 v31, v7 offset:45712
	v_add_u32_e32 v7, s14, v90
	v_max_i32_e32 v8, 8, v7
	v_min_i32_e32 v7, 0x1ff8, v7
	v_sub_u32_e32 v7, v7, v8
	v_add_u32_e32 v7, 16, v7
	v_cvt_f32_i32_e32 v7, v7
	v_rcp_iflag_f32_e32 v7, v7
	s_nop 0
	v_fma_f32 v4, v7, v6, -v4
	v_cvt_pk_bf16_f32 v4, v4, s0
	ds_write_b16 v31, v4 offset:46240
	v_max_i32_e32 v4, 8, v3
	v_min_i32_e32 v3, 0x1ff8, v3
	v_sub_u32_e32 v3, v3, v4
	v_add_u32_e32 v120, 16, v3
